# speedup vs baseline: 1.0147x; 1.0147x over previous
_Z6k_normPKfP15HIP_vector_typeIjLj4EEPfPyS4_:
	s_load_dwordx2 s[4:5], s[0:1], 0x0
	s_ashr_i32 s3, s2, 31
	s_lshl_b64 s[6:7], s[2:3], 16
	v_and_b32_e32 v1, 63, v0
	s_waitcnt lgkmcnt(0)
	s_add_u32 s4, s4, s6
	v_lshrrev_b32_e32 v66, 6, v0
	s_addc_u32 s5, s5, s7
	v_lshlrev_b32_e32 v2, 4, v1
	v_mov_b32_e32 v3, 0
	v_lshl_add_u64 v[4:5], s[4:5], 0, v[2:3]
	v_lshlrev_b32_e32 v2, 14, v66
	v_lshl_add_u64 v[2:3], v[4:5], 0, v[2:3]
	s_movk_i32 s3, 0x1000
	v_add_co_u32_e32 v68, vcc, s3, v2
	s_movk_i32 s3, 0x2000
	s_nop 0
	v_addc_co_u32_e32 v69, vcc, 0, v3, vcc
	v_add_co_u32_e32 v70, vcc, s3, v2
	global_load_dwordx4 v[62:65], v[2:3], off nt
	global_load_dwordx4 v[58:61], v[2:3], off offset:1024 nt
	global_load_dwordx4 v[50:53], v[2:3], off offset:2048 nt
	global_load_dwordx4 v[46:49], v[2:3], off offset:3072 nt
	v_addc_co_u32_e32 v71, vcc, 0, v3, vcc
	v_add_co_u32_e32 v72, vcc, 0x3000, v2
	global_load_dwordx4 v[42:45], v[68:69], off offset:1024 nt
	global_load_dwordx4 v[34:37], v[68:69], off offset:2048 nt
	global_load_dwordx4 v[30:33], v[70:71], off nt
	global_load_dwordx4 v[26:29], v[70:71], off offset:1024 nt
	global_load_dwordx4 v[22:25], v[70:71], off offset:2048 nt
	global_load_dwordx4 v[18:21], v[70:71], off offset:3072 nt
	v_addc_co_u32_e32 v73, vcc, 0, v3, vcc
	global_load_dwordx4 v[38:41], v[68:69], off offset:3072 nt
	global_load_dwordx4 v[14:17], v[72:73], off nt
	global_load_dwordx4 v[10:13], v[72:73], off offset:1024 nt
	global_load_dwordx4 v[6:9], v[72:73], off offset:2048 nt
	global_load_dwordx4 v[54:57], v[70:71], off offset:-4096 nt
	global_load_dwordx4 v[2:5], v[72:73], off offset:3072 nt
	v_cmp_gt_u32_e32 vcc, 32, v0
	s_and_saveexec_b64 s[6:7], vcc
	s_cbranch_execz .LBB0_2
	s_load_dwordx2 s[8:9], s[0:1], 0x18
	v_lshl_or_b32 v84, s2, 5, v0
	v_mov_b32_e32 v86, 0
	v_ashrrev_i32_e32 v85, 31, v84
	v_mov_b32_e32 v87, v86
	s_waitcnt lgkmcnt(0)
	v_lshl_add_u64 v[84:85], v[84:85], 3, s[8:9]
	global_store_dwordx2 v[84:85], v[86:87], off
.LBB0_2:
	s_or_b64 exec, exec, s[6:7]
	v_or_b32_e32 v83, s2, v0
	v_cmp_eq_u32_e32 vcc, 0, v83
	s_and_saveexec_b64 s[6:7], vcc
	s_cbranch_execz .LBB0_4
	s_load_dwordx2 s[8:9], s[0:1], 0x20
	v_mov_b32_e32 v83, 0
	s_waitcnt lgkmcnt(0)
	global_store_dword v83, v83, s[8:9]
.LBB0_4:
	s_or_b64 exec, exec, s[6:7]
	s_waitcnt vmcnt(14)
	v_mul_f32_e32 v67, v63, v63
	v_fmac_f32_e32 v67, v62, v62
	v_fmac_f32_e32 v67, v64, v64
	v_fmac_f32_e32 v67, v65, v65
	v_fmac_f32_e32 v67, v58, v58
	v_fmac_f32_e32 v67, v59, v59
	v_fmac_f32_e32 v67, v60, v60
	v_fmac_f32_e32 v67, v61, v61
	v_add_f32_e32 v75, v62, v63
	v_add_f32_e32 v83, v64, v65
	v_add_f32_e32 v75, v75, v83
	v_add_f32_e32 v84, v58, v59
	v_add_f32_e32 v85, v60, v61
	v_add_f32_e32 v84, v84, v85
	v_add_f32_e32 v75, v75, v84
	s_waitcnt vmcnt(12)
	v_mul_f32_e32 v68, v51, v51
	v_fmac_f32_e32 v68, v50, v50
	v_fmac_f32_e32 v68, v52, v52
	v_fmac_f32_e32 v68, v53, v53
	v_fmac_f32_e32 v68, v46, v46
	v_fmac_f32_e32 v68, v47, v47
	v_fmac_f32_e32 v68, v48, v48
	v_fmac_f32_e32 v68, v49, v49
	v_add_f32_e32 v76, v50, v51
	v_add_f32_e32 v83, v52, v53
	v_add_f32_e32 v76, v76, v83
	v_add_f32_e32 v84, v46, v47
	v_add_f32_e32 v85, v48, v49
	v_add_f32_e32 v84, v84, v85
	v_add_f32_e32 v76, v76, v84
	s_waitcnt vmcnt(8)
	v_mul_f32_e32 v71, v31, v31
	v_fmac_f32_e32 v71, v30, v30
	v_fmac_f32_e32 v71, v32, v32
	v_fmac_f32_e32 v71, v33, v33
	v_fmac_f32_e32 v71, v26, v26
	v_fmac_f32_e32 v71, v27, v27
	v_fmac_f32_e32 v71, v28, v28
	v_fmac_f32_e32 v71, v29, v29
	v_add_f32_e32 v79, v30, v31
	v_add_f32_e32 v83, v32, v33
	v_add_f32_e32 v79, v79, v83
	v_add_f32_e32 v84, v26, v27
	v_add_f32_e32 v85, v28, v29
	v_add_f32_e32 v84, v84, v85
	v_add_f32_e32 v79, v79, v84
	s_waitcnt vmcnt(6)
	v_mul_f32_e32 v72, v23, v23
	v_fmac_f32_e32 v72, v22, v22
	v_fmac_f32_e32 v72, v24, v24
	v_fmac_f32_e32 v72, v25, v25
	v_fmac_f32_e32 v72, v18, v18
	v_fmac_f32_e32 v72, v19, v19
	v_fmac_f32_e32 v72, v20, v20
	v_fmac_f32_e32 v72, v21, v21
	v_add_f32_e32 v80, v22, v23
	v_add_f32_e32 v83, v24, v25
	v_add_f32_e32 v80, v80, v83
	v_add_f32_e32 v84, v18, v19
	v_add_f32_e32 v85, v20, v21
	v_add_f32_e32 v84, v84, v85
	v_add_f32_e32 v80, v80, v84
	s_waitcnt vmcnt(5)
	v_mul_f32_e32 v70, v35, v35
	v_fmac_f32_e32 v70, v34, v34
	v_fmac_f32_e32 v70, v36, v36
	v_fmac_f32_e32 v70, v37, v37
	v_fmac_f32_e32 v70, v38, v38
	v_fmac_f32_e32 v70, v39, v39
	v_fmac_f32_e32 v70, v40, v40
	v_fmac_f32_e32 v70, v41, v41
	v_add_f32_e32 v78, v34, v35
	v_add_f32_e32 v83, v36, v37
	v_add_f32_e32 v78, v78, v83
	v_add_f32_e32 v84, v38, v39
	v_add_f32_e32 v85, v40, v41
	v_add_f32_e32 v84, v84, v85
	v_add_f32_e32 v78, v78, v84
	s_waitcnt vmcnt(3)
	v_mul_f32_e32 v73, v15, v15
	v_fmac_f32_e32 v73, v14, v14
	v_fmac_f32_e32 v73, v16, v16
	v_fmac_f32_e32 v73, v17, v17
	v_fmac_f32_e32 v73, v10, v10
	v_fmac_f32_e32 v73, v11, v11
	v_fmac_f32_e32 v73, v12, v12
	v_fmac_f32_e32 v73, v13, v13
	v_add_f32_e32 v81, v14, v15
	v_add_f32_e32 v83, v16, v17
	v_add_f32_e32 v81, v81, v83
	v_add_f32_e32 v84, v10, v11
	v_add_f32_e32 v85, v12, v13
	v_add_f32_e32 v84, v84, v85
	v_add_f32_e32 v81, v81, v84
	s_waitcnt vmcnt(1)
	v_mul_f32_e32 v69, v55, v55
	v_fmac_f32_e32 v69, v54, v54
	v_fmac_f32_e32 v69, v56, v56
	v_fmac_f32_e32 v69, v57, v57
	v_fmac_f32_e32 v69, v42, v42
	v_fmac_f32_e32 v69, v43, v43
	v_fmac_f32_e32 v69, v44, v44
	v_fmac_f32_e32 v69, v45, v45
	v_add_f32_e32 v77, v54, v55
	v_add_f32_e32 v83, v56, v57
	v_add_f32_e32 v77, v77, v83
	v_add_f32_e32 v84, v42, v43
	v_add_f32_e32 v85, v44, v45
	v_add_f32_e32 v84, v84, v85
	v_add_f32_e32 v77, v77, v84
	s_waitcnt vmcnt(0)
	v_mul_f32_e32 v74, v7, v7
	v_fmac_f32_e32 v74, v6, v6
	v_fmac_f32_e32 v74, v8, v8
	v_fmac_f32_e32 v74, v9, v9
	v_fmac_f32_e32 v74, v2, v2
	v_fmac_f32_e32 v74, v3, v3
	v_fmac_f32_e32 v74, v4, v4
	v_fmac_f32_e32 v74, v5, v5
	v_add_f32_e32 v82, v6, v7
	v_add_f32_e32 v83, v8, v9
	v_add_f32_e32 v82, v82, v83
	v_add_f32_e32 v84, v2, v3
	v_add_f32_e32 v85, v4, v5
	v_add_f32_e32 v84, v84, v85
	v_add_f32_e32 v82, v82, v84
	v_and_b32_e32 v83, 8, v0
	v_cmp_ne_u32_e64 s[6:7], 0, v83
	v_permlane32_swap_b32_e32 v67, v71
	v_permlane32_swap_b32_e32 v75, v79
	v_permlane32_swap_b32_e32 v68, v72
	v_permlane32_swap_b32_e32 v76, v80
	v_permlane32_swap_b32_e32 v69, v73
	v_permlane32_swap_b32_e32 v77, v81
	v_permlane32_swap_b32_e32 v70, v74
	v_permlane32_swap_b32_e32 v78, v82
	v_add_f32_e32 v67, v67, v71
	v_add_f32_e32 v75, v75, v79
	v_add_f32_e32 v68, v68, v72
	v_add_f32_e32 v76, v76, v80
	v_add_f32_e32 v69, v69, v73
	v_add_f32_e32 v77, v77, v81
	v_add_f32_e32 v70, v70, v74
	v_add_f32_e32 v78, v78, v82
	s_nop 1
	v_permlane16_swap_b32_e32 v67, v69
	v_permlane16_swap_b32_e32 v75, v77
	v_permlane16_swap_b32_e32 v68, v70
	v_permlane16_swap_b32_e32 v76, v78
	v_add_f32_e32 v67, v67, v69
	v_add_f32_e32 v75, v75, v77
	v_add_f32_e32 v68, v68, v70
	v_add_f32_e32 v76, v76, v78
	v_cndmask_b32_e64 v83, v67, v68, s[6:7]
	v_cndmask_b32_e64 v84, v68, v67, s[6:7]
	v_cndmask_b32_e64 v85, v75, v76, s[6:7]
	v_cndmask_b32_e64 v86, v76, v75, s[6:7]
	s_nop 1
	v_add_f32_dpp v67, v84, v83 row_ror:8 row_mask:0xf bank_mask:0xf
	v_add_f32_dpp v69, v86, v85 row_ror:8 row_mask:0xf bank_mask:0xf
	s_nop 1
	v_add_f32_dpp v67, v67, v67 row_half_mirror row_mask:0xf bank_mask:0xf
	v_add_f32_dpp v69, v69, v69 row_half_mirror row_mask:0xf bank_mask:0xf
	s_nop 1
	v_add_f32_dpp v67, v67, v67 quad_perm:[2,3,0,1] row_mask:0xf bank_mask:0xf
	v_add_f32_dpp v69, v69, v69 quad_perm:[2,3,0,1] row_mask:0xf bank_mask:0xf
	s_nop 1
	v_add_f32_dpp v67, v67, v67 quad_perm:[1,0,3,2] row_mask:0xf bank_mask:0xf
	v_add_f32_dpp v69, v69, v69 quad_perm:[1,0,3,2] row_mask:0xf bank_mask:0xf
	s_mov_b32 s3, 0xf800000
	v_mul_f32_e32 v70, 0x4f800000, v67
	v_cmp_gt_f32_e32 vcc, s3, v67
	s_nop 1
	v_cndmask_b32_e32 v67, v67, v70, vcc
	v_sqrt_f32_e32 v70, v67
	s_nop 0
	v_add_u32_e32 v68, -1, v70
	v_fma_f32 v73, -v68, v70, v67
	v_cmp_ge_f32_e64 s[4:5], 0, v73
	v_add_u32_e32 v73, 1, v70
	s_nop 0
	v_cndmask_b32_e64 v68, v70, v68, s[4:5]
	v_fma_f32 v70, -v73, v70, v67
	v_cmp_lt_f32_e64 s[4:5], 0, v70
	s_nop 1
	v_cndmask_b32_e64 v68, v68, v73, s[4:5]
	v_mul_f32_e32 v70, 0x37800000, v68
	v_cndmask_b32_e32 v68, v68, v70, vcc
	v_mov_b32_e32 v70, 0x260
	v_cmp_class_f32_e32 vcc, v67, v70
	s_nop 1
	v_cndmask_b32_e32 v67, v68, v67, vcc
	v_max_f32_e32 v68, 0x322bcc77, v67
	v_div_scale_f32 v67, s[4:5], v68, v68, 1.0
	v_rcp_f32_e32 v73, v67
	s_load_dwordx2 s[4:5], s[0:1], 0x8
	v_fma_f32 v71, -v67, v73, 1.0
	v_fmac_f32_e32 v73, v71, v73
	v_div_scale_f32 v71, vcc, 1.0, v68, 1.0
	v_mul_f32_e32 v72, v71, v73
	v_fma_f32 v74, -v67, v72, v71
	v_fmac_f32_e32 v72, v74, v73
	v_fma_f32 v67, -v67, v72, v71
	v_div_fmas_f32 v71, v67, v73, v72
	v_mov_b32_e32 v70, 0
	v_and_b32_e32 v67, 7, v0
	v_cmp_ne_u32_e32 vcc, 0, v67
	v_lshlrev_b32_e32 v67, 3, v66
	s_and_saveexec_b64 s[6:7], vcc
	s_xor_b64 s[6:7], exec, s[6:7]
	v_lshlrev_b32_e32 v67, 3, v66
	s_or_saveexec_b64 s[6:7], s[6:7]
	v_div_fixup_f32 v66, v71, v68, 1.0
	s_xor_b64 exec, exec, s[6:7]
	s_cbranch_execz .LBB0_10
	s_load_dwordx2 s[0:1], s[0:1], 0x10
	s_waitcnt lgkmcnt(0)
	v_add_f32_e32 v68, v69, v70
	v_mul_f32_e32 v70, v68, v66
	s_lshl_b32 s3, s2, 5
	v_lshrrev_b32_e32 v68, 3, v1
	v_or3_b32 v68, v67, s3, v68
	v_ashrrev_i32_e32 v69, 31, v68
	v_lshl_add_u64 v[68:69], v[68:69], 2, s[0:1]
	global_store_dword v[68:69], v70, off
